# v7 + MLA up-projection: the 40 workgroups without a uq unit take the doubled ukv units (rotation 40 instead of 216)
# speedup vs baseline: 1.0032x; 1.0032x over previous
.LBB0_2822:
	v_readlane_b32 s23, v251, 3
	v_readlane_b32 s10, v251, 2
	s_lshl_b32 s0, s23, 3
	s_lshl_b32 s33, s10, 3
	v_writelane_b32 v251, s0, 61
	s_lshl_b32 s0, s10, 4
	v_writelane_b32 v251, s0, 62
	s_add_u32 s0, s18, 0x200
	s_addc_u32 s1, s19, 0
	v_writelane_b32 v251, s0, 63
	s_waitcnt vmcnt(2)
	v_mov_b32_e32 v3, 0
	v_readlane_b32 s24, v251, 4
	v_writelane_b32 v252, s1, 0
	s_add_u32 s0, s18, 0x1000
	s_addc_u32 s1, s19, 0
	v_writelane_b32 v252, s0, 1
	v_mov_b32_e32 v220, 0x358637bd
	v_mov_b32_e32 v221, 0x260
	v_writelane_b32 v252, s1, 2
	s_add_u32 s0, s18, 0x1100
	s_addc_u32 s1, s19, 0
	v_writelane_b32 v252, s0, 3
	v_mov_b32_e32 v222, 1
	s_mov_b32 s95, 0x20000
	v_writelane_b32 v252, s1, 4
	s_add_u32 s0, s18, 0x1200
	s_addc_u32 s1, s19, 0
	v_writelane_b32 v252, s0, 5
	s_mov_b32 s94, 0x7ffffff0
	v_mov_b32_e32 v247, 0x7f800000
	v_writelane_b32 v252, s1, 6
	s_add_u32 s0, s18, 0x1300
	s_addc_u32 s1, s19, 0
	v_writelane_b32 v252, s0, 7
	s_cmp_eq_u32 s28, 15
	v_mov_b32_e32 v192, 0x3f317218
	v_writelane_b32 v252, s1, 8
	s_cselect_b64 s[0:1], -1, 0
	v_writelane_b32 v252, s0, 9
	s_cmp_eq_u32 s28, 14
	s_mov_b32 s96, 0xf800000
	v_writelane_b32 v252, s1, 10
	s_cselect_b64 s[0:1], -1, 0
	v_writelane_b32 v252, s0, 11
	s_cmp_eq_u32 s28, 13
	s_mov_b64 s[36:37], -1
	v_writelane_b32 v252, s1, 12
	s_cselect_b64 s[0:1], -1, 0
	v_writelane_b32 v252, s0, 13
	s_cmp_eq_u32 s28, 12
	s_mov_b64 s[82:83], 0x80
	v_writelane_b32 v252, s1, 14
	s_cselect_b64 s[0:1], -1, 0
	v_writelane_b32 v252, s0, 15
	s_cmp_eq_u32 s28, 11
	s_nop 0
	v_writelane_b32 v252, s1, 16
	s_cselect_b64 s[0:1], -1, 0
	v_writelane_b32 v252, s0, 17
	s_cmp_eq_u32 s28, 10
	s_nop 0
	v_writelane_b32 v252, s1, 18
	s_cselect_b64 s[0:1], -1, 0
	v_writelane_b32 v252, s0, 19
	s_cmp_eq_u32 s28, 9
	s_nop 0
	v_writelane_b32 v252, s1, 20
	s_cselect_b64 s[0:1], -1, 0
	v_writelane_b32 v252, s0, 21
	s_cmp_eq_u32 s28, 8
	s_nop 0
	v_writelane_b32 v252, s1, 22
	s_cselect_b64 s[0:1], -1, 0
	v_writelane_b32 v252, s0, 23
	s_cmp_eq_u32 s28, 7
	s_nop 0
	v_writelane_b32 v252, s1, 24
	s_cselect_b64 s[0:1], -1, 0
	v_writelane_b32 v252, s0, 25
	s_cmp_eq_u32 s28, 6
	s_nop 0
	v_writelane_b32 v252, s1, 26
	s_cselect_b64 s[0:1], -1, 0
	v_writelane_b32 v252, s0, 27
	s_cmp_eq_u32 s28, 5
	s_nop 0
	v_writelane_b32 v252, s1, 28
	s_cselect_b64 s[0:1], -1, 0
	v_writelane_b32 v252, s0, 29
	s_cmp_eq_u32 s28, 4
	s_nop 0
	v_writelane_b32 v252, s1, 30
	s_cselect_b64 s[0:1], -1, 0
	v_writelane_b32 v252, s0, 31
	s_cmp_eq_u32 s28, 3
	s_nop 0
	v_writelane_b32 v252, s1, 32
	s_cselect_b64 s[0:1], -1, 0
	v_writelane_b32 v252, s0, 33
	s_cmp_eq_u32 s28, 2
	s_nop 0
	v_writelane_b32 v252, s1, 34
	s_cselect_b64 s[0:1], -1, 0
	v_writelane_b32 v252, s0, 35
	s_cmp_eq_u32 s28, 1
	s_nop 0
	v_writelane_b32 v252, s1, 36
	s_cselect_b64 s[0:1], -1, 0
	v_writelane_b32 v252, s0, 37
	s_cmp_eq_u32 s28, 0
	s_nop 0
	v_writelane_b32 v252, s1, 38
	s_cselect_b64 s[0:1], -1, 0
	v_writelane_b32 v252, s0, 39
	s_nop 1
	v_writelane_b32 v252, s1, 40
	s_lshl_b32 s0, s28, 8
	s_add_u32 s0, s18, s0
	s_addc_u32 s1, s19, 0
	s_add_u32 s2, s0, 0x1400
	s_addc_u32 s3, s1, 0
	v_writelane_b32 v252, s2, 41
	s_add_u32 s0, s0, 0x2400
	s_addc_u32 s1, s1, 0
	v_writelane_b32 v252, s3, 42
	v_writelane_b32 v252, s0, 43
	s_nop 1
	v_writelane_b32 v252, s1, 44
	s_add_u32 s0, s18, 0x3400
	s_addc_u32 s1, s19, 0
	v_writelane_b32 v252, s0, 45
	s_nop 1
	v_writelane_b32 v252, s1, 46
	s_add_u32 s0, s18, 0x3500
	s_addc_u32 s1, s19, 0
	s_add_u32 s80, s18, 0x3cc90000
	v_writelane_b32 v252, s0, 47
	s_addc_u32 s81, s19, 0
	s_nop 0
	v_writelane_b32 v252, s1, 48
	s_add_u32 s0, s18, 0x610000
	v_writelane_b32 v252, s0, 49
	s_addc_u32 s0, s19, 0
	v_writelane_b32 v252, s0, 50
	s_add_u32 s0, s18, 0x41490000
	s_addc_u32 s1, s19, 0
	v_writelane_b32 v252, s0, 51
	s_nop 1
	v_writelane_b32 v252, s1, 52
	s_add_u32 s0, s18, 0x4b690000
	s_addc_u32 s1, s19, 0
	v_writelane_b32 v252, s0, 53
	s_nop 1
	v_writelane_b32 v252, s1, 54
	s_and_b32 s1, s23, 7
	s_ashr_i32 s0, s23, 3
	s_cmp_gt_i32 s0, 30
	s_cselect_b64 s[2:3], -1, 0
	s_cmpk_eq_i32 s10, 0x100
	s_cselect_b64 s[12:13], -1, 0
	s_and_b64 s[4:5], s[12:13], exec
	s_cselect_b32 s4, 0x340, 0
	v_writelane_b32 v252, s4, 55
	s_and_b64 s[2:3], s[2:3], s[12:13]
	v_writelane_b32 v252, s2, 56
	s_mul_i32 s6, s1, 31
	s_add_i32 s6, s6, s0
	v_writelane_b32 v252, s3, 57
	s_add_i32 s2, s0, s1
	s_sub_i32 s2, s2, 31
	v_writelane_b32 v252, s2, 58
	s_lshl_b32 s2, s1, 2
	s_sub_i32 s7, s6, s2
	s_cmpk_lg_i32 s10, 0x100
	s_cselect_b32 s2, s10, 0xf8
	s_cselect_b32 s11, s24, s6
	v_writelane_b32 v252, s2, 59
	s_cselect_b32 s2, s10, 0xd8
	s_cselect_b32 s14, s24, s7
	s_cmpk_lt_i32 s11, 0x4c0
	v_writelane_b32 v252, s2, 60
	s_cselect_b64 s[2:3], -1, 0
	v_writelane_b32 v252, s2, 61
	s_and_b32 s6, s11, 7
	s_mul_i32 s20, s1, 5
	v_writelane_b32 v252, s3, 62
	s_add_i32 s2, s11, 0xfffffb80
	s_lshr_b32 s3, s2, 3
	s_cmp_lt_u32 s2, 48
	s_cselect_b32 s4, 8, 10
	s_cmp_gt_u32 s2, 31
	s_cselect_b32 s2, s4, 2
	s_add_i32 s3, s2, s3
	s_mul_hi_i32 s2, s11, 0x38e38e39
	s_lshr_b32 s4, s2, 31
	s_ashr_i32 s2, s2, 5
	s_add_i32 s2, s2, s4
	s_mul_i32 s4, s2, 0x90
	s_sub_i32 s4, s11, s4
	s_mul_i32 s2, s2, 9
	s_and_b32 s5, s4, 7
	s_add_i32 s2, s2, s5
	s_add_i32 s8, s2, 1
	s_ashr_i32 s9, s4, 3
	s_cmp_gt_i32 s0, 26
	s_cselect_b64 s[4:5], -1, 0
	v_writelane_b32 v252, s12, 63
	s_and_b64 s[4:5], s[4:5], s[12:13]
	s_add_i32 s2, s0, s20
	v_writelane_b32 v253, s13, 0
	v_writelane_b32 v253, s4, 1
	s_sub_i32 s2, s2, 27
	s_cmpk_lt_i32 s14, 0x510
	v_writelane_b32 v253, s5, 2
	v_writelane_b32 v253, s2, 3
	s_cselect_b64 s[4:5], -1, 0
	s_mul_hi_i32 s2, s14, 0x38e38e39
	v_writelane_b32 v253, s4, 4
	s_mul_i32 s6, s6, 9
	s_nop 0
	v_writelane_b32 v253, s5, 5
	s_lshr_b32 s4, s2, 31
	s_ashr_i32 s2, s2, 5
	s_add_i32 s2, s2, s4
	s_mul_i32 s4, s2, 0x90
	s_sub_i32 s4, s14, s4
	s_lshl_b32 s2, s2, 3
	s_and_b32 s5, s4, 7
	s_or_b32 s12, s5, s2
	v_writelane_b32 v253, s14, 6
	s_mov_b32 s2, s12
	s_ashr_i32 s14, s4, 3
	v_writelane_b32 v253, s2, 7
	s_ashr_i32 s13, s12, 31
	s_ashr_i32 s15, s14, 31
	v_writelane_b32 v253, s3, 8
	s_mov_b32 s2, s14
	v_writelane_b32 v253, s2, 9
	s_lshl_b64 s[4:5], s[12:13], 20
	s_lshl_b64 s[12:13], s[14:15], 20
	v_writelane_b32 v253, s3, 10
	v_writelane_b32 v253, s12, 11
	s_add_u32 s4, s80, s4
	s_addc_u32 s5, s81, s5
	v_writelane_b32 v253, s13, 12
	s_add_u32 s12, s4, 0x80000
	v_writelane_b32 v253, s4, 13
	s_addc_u32 s13, s5, 0
	s_nop 0
	v_writelane_b32 v253, s5, 14
	v_writelane_b32 v253, s12, 15
	s_nop 1
	v_writelane_b32 v253, s13, 16
	s_add_u32 s12, s18, 0x4ec90000
	s_addc_u32 s13, s19, 0
	s_add_u32 s2, s18, 0x3a10000
	v_writelane_b32 v253, s2, 17
	s_addc_u32 s2, s19, 0
	s_add_u32 s4, s18, 0x50790000
	v_writelane_b32 v253, s2, 18
	s_addc_u32 s5, s19, 0
	v_writelane_b32 v253, s4, 19
	s_cmpk_lt_i32 s24, 0xd8
	s_mul_hi_i32 s2, s24, 0x2aaaaaab
	v_writelane_b32 v253, s5, 20
	s_cselect_b64 s[4:5], -1, 0
	v_writelane_b32 v253, s4, 21
	s_nop 1
	v_writelane_b32 v253, s5, 22
	s_lshr_b32 s4, s2, 31
	s_ashr_i32 s2, s2, 2
	s_add_i32 s2, s2, s4
	s_mul_i32 s4, s2, 24
	s_sub_i32 s4, s24, s4
	s_lshl_b32 s2, s2, 3
	s_and_b32 s5, s4, 7
	s_or_b32 s14, s5, s2
	s_mov_b32 s2, s14
	s_ashr_i32 s16, s4, 3
	v_writelane_b32 v253, s2, 23
	s_ashr_i32 s15, s14, 31
	s_ashr_i32 s17, s16, 31
	v_writelane_b32 v253, s3, 24
	s_mov_b32 s2, s16
	v_writelane_b32 v253, s2, 25
	s_lshl_b64 s[4:5], s[14:15], 18
	s_lshl_b64 s[14:15], s[16:17], 18
	v_writelane_b32 v253, s3, 26
	v_writelane_b32 v253, s14, 27
	s_add_u32 s4, s12, s4
	s_addc_u32 s5, s13, s5
	v_writelane_b32 v253, s15, 28
	v_writelane_b32 v253, s12, 29
	v_writelane_b32 v253, s13, 30
	s_add_u32 s12, s4, 0x20000
	v_writelane_b32 v253, s4, 31
	s_addc_u32 s13, s5, 0
	s_add_u32 s14, s18, 0x4fe90000
	v_writelane_b32 v253, s5, 32
	v_writelane_b32 v253, s12, 33
	s_addc_u32 s15, s19, 0
	s_add_u32 s2, s18, 0x3b90000
	v_writelane_b32 v253, s13, 34
	v_writelane_b32 v253, s2, 35
	s_addc_u32 s2, s19, 0
	s_add_i32 s21, s24, 40
	s_add_u32 s4, s18, 0x52290000
	v_writelane_b32 v253, s2, 36
	s_addc_u32 s5, s19, 0
	v_writelane_b32 v253, s4, 37
	s_cmp_lt_i32 s23, 64
	s_nop 0
	v_writelane_b32 v253, s5, 38
	s_cselect_b64 s[4:5], -1, 0
	v_writelane_b32 v253, s4, 39
	s_and_b32 s2, s23, 1
	s_bfe_u32 s12, s23, 0x20001
	v_writelane_b32 v253, s5, 40
	s_lshl_b32 s4, s2, 3
	s_add_i32 s4, s4, s0
	s_lshl_b32 s4, s4, 2
	s_or_b32 s22, s4, s12
	s_bfe_i32 s13, s23, 0x10000
	s_bitcmp1_b32 s23, 0
	s_cselect_b64 s[4:5], -1, 0
	v_writelane_b32 v253, s4, 41
	s_cmp_eq_u32 s2, 0
	s_mov_b32 s2, 0x57c90000
	v_writelane_b32 v253, s5, 42
	s_cselect_b64 s[4:5], -1, 0
	v_writelane_b32 v253, s4, 43
	s_nop 1
	v_writelane_b32 v253, s5, 44
	s_and_b64 s[4:5], s[4:5], exec
	s_cselect_b32 s2, s2, 0x5a090000
	v_writelane_b32 v253, s2, 45
	s_and_b32 s2, s13, 0xc0
	s_mul_i32 s4, s0, 0x900
	s_or_b32 s23, s2, s4
	s_lshl_b32 s2, s12, 7
	v_writelane_b32 v253, s4, 46
	s_add_u32 s4, s18, 0x5c490000
	v_writelane_b32 v253, s4, 47
	s_addc_u32 s4, s19, 0
	v_writelane_b32 v253, s4, 48
	s_add_u32 s4, s18, 0x2a10000
	v_writelane_b32 v253, s4, 49
	s_addc_u32 s4, s19, 0
	v_writelane_b32 v253, s4, 50
	s_add_u32 s4, s18, 0x33c90000
	s_addc_u32 s5, s19, 0
	v_writelane_b32 v253, s4, 51
	s_cmp_gt_i32 s0, 23
	s_cselect_b64 s[12:13], -1, 0
	v_writelane_b32 v253, s5, 52
	s_mul_i32 s4, s1, -3
	s_add_i32 s5, s7, s4
	v_writelane_b32 v253, s12, 53
	s_cmp_lg_u64 s[76:77], 0
	s_nop 0
	v_writelane_b32 v253, s13, 54
	s_cselect_b64 s[12:13], -1, 0
	s_lshl_b32 s4, s1, 3
	v_writelane_b32 v253, s12, 55
	s_add_i32 s4, s0, s4
	s_sub_i32 s4, s4, 24
	v_writelane_b32 v253, s13, 56
	v_writelane_b32 v253, s4, 57
	s_add_u32 s4, s18, 0x3c90000
	v_writelane_b32 v253, s4, 58
	s_addc_u32 s4, s19, 0
	s_add_u32 s12, s18, 0x4a8000
	v_writelane_b32 v253, s4, 59
	s_addc_u32 s13, s19, 0
	v_writelane_b32 v253, s12, 60
	s_mul_i32 s1, s1, 3
	s_nop 0
	v_writelane_b32 v253, s13, 61
	s_add_u32 s12, s18, 0x4bf90000
	s_addc_u32 s13, s19, 0
	v_writelane_b32 v253, s12, 62
	s_add_i32 s7, s24, s10
	s_nop 0
	v_writelane_b32 v253, s13, 63
	s_add_i32 s12, s7, s10
	s_add_i32 s13, s12, s10
	s_add_i32 s16, s13, s10
	s_add_i32 s17, s16, s10
	s_add_i32 s25, s17, s10
	s_add_i32 s26, s25, s10
	s_add_i32 s27, s26, s10
	s_add_i32 s28, s27, s10
	s_add_u32 s30, s18, 0x3cc90080
	s_addc_u32 s31, s19, 0
	v_writelane_b32 v254, s30, 0
	s_add_u32 s4, s18, 0x23c90000
	s_nop 0
	v_writelane_b32 v254, s31, 1
	v_writelane_b32 v254, s4, 2
	s_addc_u32 s4, s19, 0
	s_add_u32 s30, s18, 0x57c90000
	v_writelane_b32 v254, s4, 3
	s_addc_u32 s31, s19, 0
	v_writelane_b32 v254, s30, 4
	s_add_u32 s18, s18, 0x4cc000
	s_addc_u32 s19, s19, 0
	v_writelane_b32 v254, s31, 5
	v_writelane_b32 v254, s18, 6
	s_cmp_gt_i32 s0, 28
	s_nop 0
	v_writelane_b32 v254, s19, 7
	s_cselect_b64 s[18:19], -1, 0
	v_writelane_b32 v254, s18, 8
	s_add_i32 s1, s0, s1
	s_add_i32 s4, s5, s20
	v_writelane_b32 v254, s19, 9
	v_writelane_b32 v254, s5, 10
	s_sub_i32 s1, s1, 29
	v_writelane_b32 v254, s4, 11
	s_cmpk_lt_i32 s11, 0x480
	v_writelane_b32 v254, s1, 12
	s_cselect_b32 s8, s8, s6
	v_writelane_b32 v254, s11, 13
	s_mov_b32 s4, s8
	s_cselect_b32 s18, s9, s3
	v_writelane_b32 v254, s4, 14
	s_ashr_i32 s9, s8, 31
	s_ashr_i32 s19, s18, 31
	v_writelane_b32 v254, s5, 15
	s_mov_b32 s6, s18
	s_lshl_b64 s[4:5], s[8:9], 20
	v_writelane_b32 v254, s6, 16
	s_lshl_b64 s[8:9], s[18:19], 20
	s_add_u32 s4, s80, s4
	v_writelane_b32 v254, s7, 17
	v_writelane_b32 v254, s8, 18
	s_addc_u32 s5, s81, s5
	s_nop 0
	v_writelane_b32 v254, s9, 19
	s_add_u32 s8, s4, 0x80000
	v_writelane_b32 v254, s4, 20
	s_addc_u32 s9, s5, 0
	s_abs_i32 s1, s10
	v_cvt_f32_u32_e32 v1, s1
	v_writelane_b32 v254, s5, 21
	s_sub_i32 s3, 0, s1
	v_writelane_b32 v254, s8, 22
	v_rcp_iflag_f32_e32 v1, v1
	s_lshl_b32 s0, s0, 6
	v_writelane_b32 v254, s9, 23
	s_addk_i32 s0, 0x800
	v_mul_f32_e32 v1, 0x4f7ffffe, v1
	v_cvt_u32_f32_e32 v1, v1
	v_writelane_b32 v254, s0, 24
	s_ashr_i32 s0, s21, 31
	v_readfirstlane_b32 s4, v1
	s_mul_i32 s3, s3, s4
	s_mul_hi_u32 s3, s4, s3
	s_add_i32 s4, s4, s3
	s_abs_i32 s3, s21
	s_mul_hi_u32 s4, s3, s4
	s_mul_i32 s4, s4, s1
	s_sub_i32 s3, s3, s4
	s_sub_i32 s4, s3, s1
	s_cmp_ge_u32 s3, s1
	s_cselect_b32 s3, s4, s3
	s_sub_i32 s4, s3, s1
	s_cmp_ge_u32 s3, s1
	s_cselect_b32 s1, s4, s3
	s_xor_b32 s1, s1, s0
	s_sub_i32 s3, s1, s0
	s_cmpk_lt_i32 s3, 0x120
	s_cselect_b64 s[0:1], -1, 0
	v_writelane_b32 v254, s0, 25
	v_mbcnt_lo_u32_b32 v1, -1, 0
	s_nop 0
	v_writelane_b32 v254, s1, 26
	s_ashr_i32 s0, s3, 31
	s_lshr_b32 s0, s0, 27
	s_add_i32 s0, s3, s0
	s_ashr_i32 s1, s0, 5
	s_andn2_b32 s0, s0, 31
	s_sub_i32 s0, s3, s0
	v_writelane_b32 v254, s3, 27
	s_lshl_b32 s1, s1, 3
	s_and_b32 s3, s0, 7
	s_or_b32 s4, s3, s1
	s_ashr_i32 s8, s0, 3
	s_mov_b32 s0, s4
	s_ashr_i32 s5, s4, 31
	v_writelane_b32 v254, s0, 28
	s_ashr_i32 s9, s8, 31
	s_mul_hi_i32 s3, s23, 0x2400
	v_writelane_b32 v254, s1, 29
	s_lshl_b64 s[0:1], s[4:5], 17
	s_mov_b32 s4, s8
	v_writelane_b32 v254, s4, 30
	v_mbcnt_hi_u32_b32 v224, -1, v1
	s_nop 0
	v_writelane_b32 v254, s5, 31
	s_lshl_b64 s[4:5], s[8:9], 17
	v_writelane_b32 v254, s4, 32
	s_nop 1
	v_writelane_b32 v254, s5, 33
	v_writelane_b32 v254, s14, 34
	v_writelane_b32 v254, s15, 35
	s_add_u32 s4, s14, s0
	v_writelane_b32 v254, s3, 36
	s_mul_i32 s3, s23, 0x2400
	s_addc_u32 s5, s15, s1
	v_writelane_b32 v254, s3, 37
	s_add_u32 s8, s4, 0x10000
	v_writelane_b32 v254, s4, 38
	s_addc_u32 s9, s5, 0
	s_mul_hi_i32 s1, s22, 0x900
	v_writelane_b32 v254, s5, 39
	s_mul_i32 s0, s22, 0x900
	v_writelane_b32 v254, s8, 40
	s_lshl_b64 s[0:1], s[0:1], 2
	s_nop 0
	v_writelane_b32 v254, s9, 41
	v_writelane_b32 v254, s0, 42
	s_nop 1
	v_writelane_b32 v254, s1, 43
	s_lshl_b32 s0, s2, 1
	v_writelane_b32 v254, s0, 44
	s_ashr_i32 s0, s24, 31
	v_writelane_b32 v254, s0, 45
	s_abs_i32 s0, s24
	v_writelane_b32 v254, s0, 46
	s_ashr_i32 s0, s7, 31
	v_writelane_b32 v254, s0, 47
	v_writelane_b32 v254, s7, 48
	s_abs_i32 s0, s7
	v_writelane_b32 v254, s0, 49
	s_ashr_i32 s0, s12, 31
	v_writelane_b32 v254, s0, 50
	v_writelane_b32 v254, s12, 51
	s_abs_i32 s0, s12
	v_writelane_b32 v254, s0, 52
	s_ashr_i32 s0, s13, 31
	v_writelane_b32 v254, s0, 53
	v_writelane_b32 v254, s13, 54
	s_abs_i32 s0, s13
	v_writelane_b32 v254, s0, 55
	s_ashr_i32 s0, s16, 31
	v_writelane_b32 v254, s0, 56
	v_writelane_b32 v254, s16, 57
	s_abs_i32 s0, s16
	v_writelane_b32 v254, s0, 58
	s_ashr_i32 s0, s17, 31
	v_writelane_b32 v254, s0, 59
	v_writelane_b32 v254, s17, 60
	s_abs_i32 s0, s17
	v_writelane_b32 v254, s0, 61
	s_ashr_i32 s0, s25, 31
	v_writelane_b32 v254, s0, 62
	s_abs_i32 s0, s25
	v_writelane_b32 v255, s0, 0
	s_ashr_i32 s0, s26, 31
	v_writelane_b32 v255, s0, 1
	v_writelane_b32 v255, s26, 2
	s_abs_i32 s0, s26
	v_writelane_b32 v255, s0, 3
	s_ashr_i32 s0, s27, 31
	v_writelane_b32 v255, s0, 4
	v_writelane_b32 v255, s27, 5
	s_abs_i32 s0, s27
	v_writelane_b32 v255, s0, 6
	s_ashr_i32 s0, s28, 31
	v_writelane_b32 v255, s0, 7
	v_writelane_b32 v255, s28, 8
	s_abs_i32 s0, s28
	v_writelane_b32 v255, s0, 9
	s_mul_i32 s0, s10, 24
	v_writelane_b32 v255, s0, 10
	s_add_i32 s0, 0, 0x25fc0
	v_writelane_b32 v255, s0, 11
	s_add_i32 s0, 0, 0x25fc4
	v_writelane_b32 v255, s0, 12
	s_add_i32 s0, 0, 0x1e800
	v_writelane_b32 v255, s0, 13
	s_add_i32 s0, 0, 0x21700
	v_writelane_b32 v255, s0, 14
	s_add_i32 s0, 0, 0x21600
	v_writelane_b32 v255, s0, 15
	s_add_i32 s0, 0, 0x20e00
	v_writelane_b32 v255, s0, 16
	s_add_i32 s0, 0, 0x11c00
	v_writelane_b32 v255, s0, 17
	s_add_i32 s0, 0, 0x25fd0
	v_writelane_b32 v255, s0, 18
	s_add_i32 s0, 0, 0x20200
	s_mov_b32 s7, 0
	v_writelane_b32 v254, s25, 63
	v_writelane_b32 v255, s0, 19
	s_mov_b32 s2, s7
	s_branch .LBB0_2826
